# P0 adaLN unit: cond staging loop (32 dependent load->silu->ds_write round trips) unrolled with all 32 loads in flight and counted vmcnt waits
# speedup vs baseline: 1.0018x; 1.0018x over previous
; DI const float* inp(kptr_t k, int i) { return (const float*)k[i]; }
; DI void p_adaln_unit(Frame& F, int unit) {
;     ...
;     for (int i = F.tid; i < NB * D; i += 512) { const int b = i / D, k = i % D; const float v = inp(KA, I_C)[i]; condT[k * 16 + b] = v / (1.0f + __expf(-v)); }
.LBB0_8:
	s_mov_b32 s4, -1
	s_mov_b32 s97, s12
	s_nop 0
	v_mbcnt_lo_u32_b32 v0, s4, 0
	v_mbcnt_hi_u32_b32 v2, s4, v0
	v_readlane_b32 s4, v253, 29
	v_readlane_b32 s5, v253, 30
	v_lshl_add_u32 v0, s97, 6, v2
	v_readlane_b32 s4, v253, 6
	v_readlane_b32 s5, v253, 7
	v_cmp_gt_i32_e32 vcc, s95, v0
	s_and_saveexec_b64 s[6:7], vcc
	s_cbranch_execz .LBB0_11
	s_load_dwordx2 s[8:9], s[4:5], 0x8
	v_lshl_add_u32 v3, v0, 6, 0
	v_lshlrev_b32_e32 v4, 2, v0
	s_waitcnt lgkmcnt(0)
	global_load_dword v24, v4, s[8:9]
	global_load_dword v25, v4, s[8:9] offset:2048
	s_add_u32 s8, s8, 0x1000
	s_addc_u32 s9, s9, 0
	global_load_dword v26, v4, s[8:9]
	global_load_dword v27, v4, s[8:9] offset:2048
	s_add_u32 s8, s8, 0x1000
	s_addc_u32 s9, s9, 0
	global_load_dword v28, v4, s[8:9]
	global_load_dword v29, v4, s[8:9] offset:2048
	s_add_u32 s8, s8, 0x1000
	s_addc_u32 s9, s9, 0
	global_load_dword v30, v4, s[8:9]
	global_load_dword v31, v4, s[8:9] offset:2048
	s_add_u32 s8, s8, 0x1000
	s_addc_u32 s9, s9, 0
	global_load_dword v32, v4, s[8:9]
	global_load_dword v33, v4, s[8:9] offset:2048
	s_add_u32 s8, s8, 0x1000
	s_addc_u32 s9, s9, 0
	global_load_dword v34, v4, s[8:9]
	global_load_dword v35, v4, s[8:9] offset:2048
	s_add_u32 s8, s8, 0x1000
	s_addc_u32 s9, s9, 0
	global_load_dword v36, v4, s[8:9]
	global_load_dword v37, v4, s[8:9] offset:2048
	s_add_u32 s8, s8, 0x1000
	s_addc_u32 s9, s9, 0
	global_load_dword v38, v4, s[8:9]
	global_load_dword v39, v4, s[8:9] offset:2048
	s_add_u32 s8, s8, 0x1000
	s_addc_u32 s9, s9, 0
	global_load_dword v40, v4, s[8:9]
	global_load_dword v41, v4, s[8:9] offset:2048
	s_add_u32 s8, s8, 0x1000
	s_addc_u32 s9, s9, 0
	global_load_dword v42, v4, s[8:9]
	global_load_dword v43, v4, s[8:9] offset:2048
	s_add_u32 s8, s8, 0x1000
	s_addc_u32 s9, s9, 0
	global_load_dword v44, v4, s[8:9]
	global_load_dword v45, v4, s[8:9] offset:2048
	s_add_u32 s8, s8, 0x1000
	s_addc_u32 s9, s9, 0
	global_load_dword v46, v4, s[8:9]
	global_load_dword v47, v4, s[8:9] offset:2048
	s_add_u32 s8, s8, 0x1000
	s_addc_u32 s9, s9, 0
	global_load_dword v48, v4, s[8:9]
	global_load_dword v49, v4, s[8:9] offset:2048
	s_add_u32 s8, s8, 0x1000
	s_addc_u32 s9, s9, 0
	global_load_dword v50, v4, s[8:9]
	global_load_dword v51, v4, s[8:9] offset:2048
	s_add_u32 s8, s8, 0x1000
	s_addc_u32 s9, s9, 0
	global_load_dword v52, v4, s[8:9]
	global_load_dword v53, v4, s[8:9] offset:2048
	s_add_u32 s8, s8, 0x1000
	s_addc_u32 s9, s9, 0
	global_load_dword v54, v4, s[8:9]
	global_load_dword v55, v4, s[8:9] offset:2048
	s_waitcnt vmcnt(31)
	v_mul_f32_e32 v10, 0xbfb8aa3b, v24
	v_exp_f32_e32 v10, v10
	s_nop 0
	v_add_f32_e32 v10, 1.0, v10
	v_div_scale_f32 v11, s[10:11], v10, v10, v24
	v_rcp_f32_e32 v12, v11
	s_nop 0
	v_fma_f32 v13, -v11, v12, 1.0
	v_fmac_f32_e32 v12, v13, v12
	v_div_scale_f32 v13, vcc, v24, v10, v24
	v_mul_f32_e32 v14, v13, v12
	v_fma_f32 v15, -v11, v14, v13
	v_fmac_f32_e32 v14, v15, v12
	v_fma_f32 v11, -v11, v14, v13
	v_div_fmas_f32 v11, v11, v12, v14
	v_div_fixup_f32 v24, v11, v10, v24
	ds_write_b32 v3, v24
	s_waitcnt vmcnt(30)
	v_mul_f32_e32 v10, 0xbfb8aa3b, v25
	v_exp_f32_e32 v10, v10
	s_nop 0
	v_add_f32_e32 v10, 1.0, v10
	v_div_scale_f32 v11, s[10:11], v10, v10, v25
	v_rcp_f32_e32 v12, v11
	s_nop 0
	v_fma_f32 v13, -v11, v12, 1.0
	v_fmac_f32_e32 v12, v13, v12
	v_div_scale_f32 v13, vcc, v25, v10, v25
	v_mul_f32_e32 v14, v13, v12
	v_fma_f32 v15, -v11, v14, v13
	v_fmac_f32_e32 v14, v15, v12
	v_fma_f32 v11, -v11, v14, v13
	v_div_fmas_f32 v11, v11, v12, v14
	v_div_fixup_f32 v25, v11, v10, v25
	ds_write_b32 v3, v25 offset:32768
	s_waitcnt vmcnt(29)
	v_mul_f32_e32 v10, 0xbfb8aa3b, v26
	v_exp_f32_e32 v10, v10
	s_nop 0
	v_add_f32_e32 v10, 1.0, v10
	v_div_scale_f32 v11, s[10:11], v10, v10, v26
	v_rcp_f32_e32 v12, v11
	s_nop 0
	v_fma_f32 v13, -v11, v12, 1.0
	v_fmac_f32_e32 v12, v13, v12
	v_div_scale_f32 v13, vcc, v26, v10, v26
	v_mul_f32_e32 v14, v13, v12
	v_fma_f32 v15, -v11, v14, v13
	v_fmac_f32_e32 v14, v15, v12
	v_fma_f32 v11, -v11, v14, v13
	v_div_fmas_f32 v11, v11, v12, v14
	v_div_fixup_f32 v26, v11, v10, v26
	ds_write_b32 v3, v26 offset:4
	s_waitcnt vmcnt(28)
	v_mul_f32_e32 v10, 0xbfb8aa3b, v27
	v_exp_f32_e32 v10, v10
	s_nop 0
	v_add_f32_e32 v10, 1.0, v10
	v_div_scale_f32 v11, s[10:11], v10, v10, v27
	v_rcp_f32_e32 v12, v11
	s_nop 0
	v_fma_f32 v13, -v11, v12, 1.0
	v_fmac_f32_e32 v12, v13, v12
	v_div_scale_f32 v13, vcc, v27, v10, v27
	v_mul_f32_e32 v14, v13, v12
	v_fma_f32 v15, -v11, v14, v13
	v_fmac_f32_e32 v14, v15, v12
	v_fma_f32 v11, -v11, v14, v13
	v_div_fmas_f32 v11, v11, v12, v14
	v_div_fixup_f32 v27, v11, v10, v27
	ds_write_b32 v3, v27 offset:32772
	s_waitcnt vmcnt(27)
	v_mul_f32_e32 v10, 0xbfb8aa3b, v28
	v_exp_f32_e32 v10, v10
	s_nop 0
	v_add_f32_e32 v10, 1.0, v10
	v_div_scale_f32 v11, s[10:11], v10, v10, v28
	v_rcp_f32_e32 v12, v11
	s_nop 0
	v_fma_f32 v13, -v11, v12, 1.0
	v_fmac_f32_e32 v12, v13, v12
	v_div_scale_f32 v13, vcc, v28, v10, v28
	v_mul_f32_e32 v14, v13, v12
	v_fma_f32 v15, -v11, v14, v13
	v_fmac_f32_e32 v14, v15, v12
	v_fma_f32 v11, -v11, v14, v13
	v_div_fmas_f32 v11, v11, v12, v14
	v_div_fixup_f32 v28, v11, v10, v28
	ds_write_b32 v3, v28 offset:8
	s_waitcnt vmcnt(26)
	v_mul_f32_e32 v10, 0xbfb8aa3b, v29
	v_exp_f32_e32 v10, v10
	s_nop 0
	v_add_f32_e32 v10, 1.0, v10
	v_div_scale_f32 v11, s[10:11], v10, v10, v29
	v_rcp_f32_e32 v12, v11
	s_nop 0
	v_fma_f32 v13, -v11, v12, 1.0
	v_fmac_f32_e32 v12, v13, v12
	v_div_scale_f32 v13, vcc, v29, v10, v29
	v_mul_f32_e32 v14, v13, v12
	v_fma_f32 v15, -v11, v14, v13
	v_fmac_f32_e32 v14, v15, v12
	v_fma_f32 v11, -v11, v14, v13
	v_div_fmas_f32 v11, v11, v12, v14
	v_div_fixup_f32 v29, v11, v10, v29
	ds_write_b32 v3, v29 offset:32776
	s_waitcnt vmcnt(25)
; DI const float* inp(kptr_t k, int i) { return (const float*)k[i]; }
; DI void p_adaln_unit(Frame& F, int unit) {
;     ...
;     for (int i = F.tid; i < NB * D; i += 512) { const int b = i / D, k = i % D; const float v = inp(KA, I_C)[i]; condT[k * 16 + b] = v / (1.0f + __expf(-v)); }
	v_mul_f32_e32 v10, 0xbfb8aa3b, v30
	v_exp_f32_e32 v10, v10
	s_nop 0
	v_add_f32_e32 v10, 1.0, v10
	v_div_scale_f32 v11, s[10:11], v10, v10, v30
	v_rcp_f32_e32 v12, v11
	s_nop 0
	v_fma_f32 v13, -v11, v12, 1.0
	v_fmac_f32_e32 v12, v13, v12
	v_div_scale_f32 v13, vcc, v30, v10, v30
	v_mul_f32_e32 v14, v13, v12
	v_fma_f32 v15, -v11, v14, v13
	v_fmac_f32_e32 v14, v15, v12
	v_fma_f32 v11, -v11, v14, v13
	v_div_fmas_f32 v11, v11, v12, v14
	v_div_fixup_f32 v30, v11, v10, v30
	ds_write_b32 v3, v30 offset:12
	s_waitcnt vmcnt(24)
	v_mul_f32_e32 v10, 0xbfb8aa3b, v31
	v_exp_f32_e32 v10, v10
	s_nop 0
	v_add_f32_e32 v10, 1.0, v10
	v_div_scale_f32 v11, s[10:11], v10, v10, v31
	v_rcp_f32_e32 v12, v11
	s_nop 0
	v_fma_f32 v13, -v11, v12, 1.0
	v_fmac_f32_e32 v12, v13, v12
	v_div_scale_f32 v13, vcc, v31, v10, v31
	v_mul_f32_e32 v14, v13, v12
	v_fma_f32 v15, -v11, v14, v13
	v_fmac_f32_e32 v14, v15, v12
	v_fma_f32 v11, -v11, v14, v13
	v_div_fmas_f32 v11, v11, v12, v14
	v_div_fixup_f32 v31, v11, v10, v31
	ds_write_b32 v3, v31 offset:32780
	s_waitcnt vmcnt(23)
	v_mul_f32_e32 v10, 0xbfb8aa3b, v32
	v_exp_f32_e32 v10, v10
	s_nop 0
	v_add_f32_e32 v10, 1.0, v10
	v_div_scale_f32 v11, s[10:11], v10, v10, v32
	v_rcp_f32_e32 v12, v11
	s_nop 0
	v_fma_f32 v13, -v11, v12, 1.0
	v_fmac_f32_e32 v12, v13, v12
	v_div_scale_f32 v13, vcc, v32, v10, v32
	v_mul_f32_e32 v14, v13, v12
	v_fma_f32 v15, -v11, v14, v13
	v_fmac_f32_e32 v14, v15, v12
	v_fma_f32 v11, -v11, v14, v13
	v_div_fmas_f32 v11, v11, v12, v14
	v_div_fixup_f32 v32, v11, v10, v32
	ds_write_b32 v3, v32 offset:16
	s_waitcnt vmcnt(22)
	v_mul_f32_e32 v10, 0xbfb8aa3b, v33
	v_exp_f32_e32 v10, v10
	s_nop 0
	v_add_f32_e32 v10, 1.0, v10
	v_div_scale_f32 v11, s[10:11], v10, v10, v33
	v_rcp_f32_e32 v12, v11
	s_nop 0
	v_fma_f32 v13, -v11, v12, 1.0
	v_fmac_f32_e32 v12, v13, v12
	v_div_scale_f32 v13, vcc, v33, v10, v33
	v_mul_f32_e32 v14, v13, v12
	v_fma_f32 v15, -v11, v14, v13
	v_fmac_f32_e32 v14, v15, v12
	v_fma_f32 v11, -v11, v14, v13
	v_div_fmas_f32 v11, v11, v12, v14
	v_div_fixup_f32 v33, v11, v10, v33
	ds_write_b32 v3, v33 offset:32784
	s_waitcnt vmcnt(21)
	v_mul_f32_e32 v10, 0xbfb8aa3b, v34
	v_exp_f32_e32 v10, v10
	s_nop 0
	v_add_f32_e32 v10, 1.0, v10
	v_div_scale_f32 v11, s[10:11], v10, v10, v34
	v_rcp_f32_e32 v12, v11
	s_nop 0
	v_fma_f32 v13, -v11, v12, 1.0
	v_fmac_f32_e32 v12, v13, v12
	v_div_scale_f32 v13, vcc, v34, v10, v34
	v_mul_f32_e32 v14, v13, v12
	v_fma_f32 v15, -v11, v14, v13
	v_fmac_f32_e32 v14, v15, v12
	v_fma_f32 v11, -v11, v14, v13
	v_div_fmas_f32 v11, v11, v12, v14
	v_div_fixup_f32 v34, v11, v10, v34
	ds_write_b32 v3, v34 offset:20
	s_waitcnt vmcnt(20)
	v_mul_f32_e32 v10, 0xbfb8aa3b, v35
	v_exp_f32_e32 v10, v10
	s_nop 0
	v_add_f32_e32 v10, 1.0, v10
	v_div_scale_f32 v11, s[10:11], v10, v10, v35
	v_rcp_f32_e32 v12, v11
	s_nop 0
	v_fma_f32 v13, -v11, v12, 1.0
	v_fmac_f32_e32 v12, v13, v12
	v_div_scale_f32 v13, vcc, v35, v10, v35
	v_mul_f32_e32 v14, v13, v12
	v_fma_f32 v15, -v11, v14, v13
	v_fmac_f32_e32 v14, v15, v12
	v_fma_f32 v11, -v11, v14, v13
	v_div_fmas_f32 v11, v11, v12, v14
	v_div_fixup_f32 v35, v11, v10, v35
	ds_write_b32 v3, v35 offset:32788
	s_waitcnt vmcnt(19)
	v_mul_f32_e32 v10, 0xbfb8aa3b, v36
	v_exp_f32_e32 v10, v10
	s_nop 0
	v_add_f32_e32 v10, 1.0, v10
	v_div_scale_f32 v11, s[10:11], v10, v10, v36
	v_rcp_f32_e32 v12, v11
	s_nop 0
	v_fma_f32 v13, -v11, v12, 1.0
	v_fmac_f32_e32 v12, v13, v12
	v_div_scale_f32 v13, vcc, v36, v10, v36
	v_mul_f32_e32 v14, v13, v12
	v_fma_f32 v15, -v11, v14, v13
	v_fmac_f32_e32 v14, v15, v12
	v_fma_f32 v11, -v11, v14, v13
	v_div_fmas_f32 v11, v11, v12, v14
	v_div_fixup_f32 v36, v11, v10, v36
	ds_write_b32 v3, v36 offset:24
	s_waitcnt vmcnt(18)
	v_mul_f32_e32 v10, 0xbfb8aa3b, v37
	v_exp_f32_e32 v10, v10
	s_nop 0
	v_add_f32_e32 v10, 1.0, v10
	v_div_scale_f32 v11, s[10:11], v10, v10, v37
	v_rcp_f32_e32 v12, v11
	s_nop 0
	v_fma_f32 v13, -v11, v12, 1.0
	v_fmac_f32_e32 v12, v13, v12
	v_div_scale_f32 v13, vcc, v37, v10, v37
	v_mul_f32_e32 v14, v13, v12
	v_fma_f32 v15, -v11, v14, v13
	v_fmac_f32_e32 v14, v15, v12
	v_fma_f32 v11, -v11, v14, v13
	v_div_fmas_f32 v11, v11, v12, v14
	v_div_fixup_f32 v37, v11, v10, v37
	ds_write_b32 v3, v37 offset:32792
	s_waitcnt vmcnt(17)
	v_mul_f32_e32 v10, 0xbfb8aa3b, v38
	v_exp_f32_e32 v10, v10
	s_nop 0
	v_add_f32_e32 v10, 1.0, v10
	v_div_scale_f32 v11, s[10:11], v10, v10, v38
	v_rcp_f32_e32 v12, v11
	s_nop 0
	v_fma_f32 v13, -v11, v12, 1.0
	v_fmac_f32_e32 v12, v13, v12
	v_div_scale_f32 v13, vcc, v38, v10, v38
	v_mul_f32_e32 v14, v13, v12
	v_fma_f32 v15, -v11, v14, v13
	v_fmac_f32_e32 v14, v15, v12
	v_fma_f32 v11, -v11, v14, v13
	v_div_fmas_f32 v11, v11, v12, v14
	v_div_fixup_f32 v38, v11, v10, v38
	ds_write_b32 v3, v38 offset:28
	s_waitcnt vmcnt(16)
	v_mul_f32_e32 v10, 0xbfb8aa3b, v39
	v_exp_f32_e32 v10, v10
	s_nop 0
	v_add_f32_e32 v10, 1.0, v10
	v_div_scale_f32 v11, s[10:11], v10, v10, v39
	v_rcp_f32_e32 v12, v11
	s_nop 0
	v_fma_f32 v13, -v11, v12, 1.0
	v_fmac_f32_e32 v12, v13, v12
	v_div_scale_f32 v13, vcc, v39, v10, v39
	v_mul_f32_e32 v14, v13, v12
	v_fma_f32 v15, -v11, v14, v13
	v_fmac_f32_e32 v14, v15, v12
	v_fma_f32 v11, -v11, v14, v13
	v_div_fmas_f32 v11, v11, v12, v14
	v_div_fixup_f32 v39, v11, v10, v39
	ds_write_b32 v3, v39 offset:32796
	s_waitcnt vmcnt(15)
	v_mul_f32_e32 v10, 0xbfb8aa3b, v40
	v_exp_f32_e32 v10, v10
	s_nop 0
	v_add_f32_e32 v10, 1.0, v10
	v_div_scale_f32 v11, s[10:11], v10, v10, v40
	v_rcp_f32_e32 v12, v11
	s_nop 0
	v_fma_f32 v13, -v11, v12, 1.0
	v_fmac_f32_e32 v12, v13, v12
	v_div_scale_f32 v13, vcc, v40, v10, v40
	v_mul_f32_e32 v14, v13, v12
	v_fma_f32 v15, -v11, v14, v13
	v_fmac_f32_e32 v14, v15, v12
	v_fma_f32 v11, -v11, v14, v13
	v_div_fmas_f32 v11, v11, v12, v14
	v_div_fixup_f32 v40, v11, v10, v40
	ds_write_b32 v3, v40 offset:32
	s_waitcnt vmcnt(14)
; DI const float* inp(kptr_t k, int i) { return (const float*)k[i]; }
; DI void p_adaln_unit(Frame& F, int unit) {
;     ...
;     for (int i = F.tid; i < NB * D; i += 512) { const int b = i / D, k = i % D; const float v = inp(KA, I_C)[i]; condT[k * 16 + b] = v / (1.0f + __expf(-v)); }
	v_mul_f32_e32 v10, 0xbfb8aa3b, v41
	v_exp_f32_e32 v10, v10
	s_nop 0
	v_add_f32_e32 v10, 1.0, v10
	v_div_scale_f32 v11, s[10:11], v10, v10, v41
	v_rcp_f32_e32 v12, v11
	s_nop 0
	v_fma_f32 v13, -v11, v12, 1.0
	v_fmac_f32_e32 v12, v13, v12
	v_div_scale_f32 v13, vcc, v41, v10, v41
	v_mul_f32_e32 v14, v13, v12
	v_fma_f32 v15, -v11, v14, v13
	v_fmac_f32_e32 v14, v15, v12
	v_fma_f32 v11, -v11, v14, v13
	v_div_fmas_f32 v11, v11, v12, v14
	v_div_fixup_f32 v41, v11, v10, v41
	ds_write_b32 v3, v41 offset:32800
	s_waitcnt vmcnt(13)
	v_mul_f32_e32 v10, 0xbfb8aa3b, v42
	v_exp_f32_e32 v10, v10
	s_nop 0
	v_add_f32_e32 v10, 1.0, v10
	v_div_scale_f32 v11, s[10:11], v10, v10, v42
	v_rcp_f32_e32 v12, v11
	s_nop 0
	v_fma_f32 v13, -v11, v12, 1.0
	v_fmac_f32_e32 v12, v13, v12
	v_div_scale_f32 v13, vcc, v42, v10, v42
	v_mul_f32_e32 v14, v13, v12
	v_fma_f32 v15, -v11, v14, v13
	v_fmac_f32_e32 v14, v15, v12
	v_fma_f32 v11, -v11, v14, v13
	v_div_fmas_f32 v11, v11, v12, v14
	v_div_fixup_f32 v42, v11, v10, v42
	ds_write_b32 v3, v42 offset:36
	s_waitcnt vmcnt(12)
	v_mul_f32_e32 v10, 0xbfb8aa3b, v43
	v_exp_f32_e32 v10, v10
	s_nop 0
	v_add_f32_e32 v10, 1.0, v10
	v_div_scale_f32 v11, s[10:11], v10, v10, v43
	v_rcp_f32_e32 v12, v11
	s_nop 0
	v_fma_f32 v13, -v11, v12, 1.0
	v_fmac_f32_e32 v12, v13, v12
	v_div_scale_f32 v13, vcc, v43, v10, v43
	v_mul_f32_e32 v14, v13, v12
	v_fma_f32 v15, -v11, v14, v13
	v_fmac_f32_e32 v14, v15, v12
	v_fma_f32 v11, -v11, v14, v13
	v_div_fmas_f32 v11, v11, v12, v14
	v_div_fixup_f32 v43, v11, v10, v43
	ds_write_b32 v3, v43 offset:32804
	s_waitcnt vmcnt(11)
	v_mul_f32_e32 v10, 0xbfb8aa3b, v44
	v_exp_f32_e32 v10, v10
	s_nop 0
	v_add_f32_e32 v10, 1.0, v10
	v_div_scale_f32 v11, s[10:11], v10, v10, v44
	v_rcp_f32_e32 v12, v11
	s_nop 0
	v_fma_f32 v13, -v11, v12, 1.0
	v_fmac_f32_e32 v12, v13, v12
	v_div_scale_f32 v13, vcc, v44, v10, v44
	v_mul_f32_e32 v14, v13, v12
	v_fma_f32 v15, -v11, v14, v13
	v_fmac_f32_e32 v14, v15, v12
	v_fma_f32 v11, -v11, v14, v13
	v_div_fmas_f32 v11, v11, v12, v14
	v_div_fixup_f32 v44, v11, v10, v44
	ds_write_b32 v3, v44 offset:40
	s_waitcnt vmcnt(10)
	v_mul_f32_e32 v10, 0xbfb8aa3b, v45
	v_exp_f32_e32 v10, v10
	s_nop 0
	v_add_f32_e32 v10, 1.0, v10
	v_div_scale_f32 v11, s[10:11], v10, v10, v45
	v_rcp_f32_e32 v12, v11
	s_nop 0
	v_fma_f32 v13, -v11, v12, 1.0
	v_fmac_f32_e32 v12, v13, v12
	v_div_scale_f32 v13, vcc, v45, v10, v45
	v_mul_f32_e32 v14, v13, v12
	v_fma_f32 v15, -v11, v14, v13
	v_fmac_f32_e32 v14, v15, v12
	v_fma_f32 v11, -v11, v14, v13
	v_div_fmas_f32 v11, v11, v12, v14
	v_div_fixup_f32 v45, v11, v10, v45
	ds_write_b32 v3, v45 offset:32808
	s_waitcnt vmcnt(9)
	v_mul_f32_e32 v10, 0xbfb8aa3b, v46
	v_exp_f32_e32 v10, v10
	s_nop 0
	v_add_f32_e32 v10, 1.0, v10
	v_div_scale_f32 v11, s[10:11], v10, v10, v46
	v_rcp_f32_e32 v12, v11
	s_nop 0
	v_fma_f32 v13, -v11, v12, 1.0
	v_fmac_f32_e32 v12, v13, v12
	v_div_scale_f32 v13, vcc, v46, v10, v46
	v_mul_f32_e32 v14, v13, v12
	v_fma_f32 v15, -v11, v14, v13
	v_fmac_f32_e32 v14, v15, v12
	v_fma_f32 v11, -v11, v14, v13
	v_div_fmas_f32 v11, v11, v12, v14
	v_div_fixup_f32 v46, v11, v10, v46
	ds_write_b32 v3, v46 offset:44
	s_waitcnt vmcnt(8)
	v_mul_f32_e32 v10, 0xbfb8aa3b, v47
	v_exp_f32_e32 v10, v10
	s_nop 0
	v_add_f32_e32 v10, 1.0, v10
	v_div_scale_f32 v11, s[10:11], v10, v10, v47
	v_rcp_f32_e32 v12, v11
	s_nop 0
	v_fma_f32 v13, -v11, v12, 1.0
	v_fmac_f32_e32 v12, v13, v12
	v_div_scale_f32 v13, vcc, v47, v10, v47
	v_mul_f32_e32 v14, v13, v12
	v_fma_f32 v15, -v11, v14, v13
	v_fmac_f32_e32 v14, v15, v12
	v_fma_f32 v11, -v11, v14, v13
	v_div_fmas_f32 v11, v11, v12, v14
	v_div_fixup_f32 v47, v11, v10, v47
	ds_write_b32 v3, v47 offset:32812
	s_waitcnt vmcnt(7)
; DI const float* inp(kptr_t k, int i) { return (const float*)k[i]; }
; DI void p_adaln_unit(Frame& F, int unit) {
;     ...
;     for (int i = F.tid; i < NB * D; i += 512) { const int b = i / D, k = i % D; const float v = inp(KA, I_C)[i]; condT[k * 16 + b] = v / (1.0f + __expf(-v)); }
	v_mul_f32_e32 v10, 0xbfb8aa3b, v48
	v_exp_f32_e32 v10, v10
	s_nop 0
	v_add_f32_e32 v10, 1.0, v10
	v_div_scale_f32 v11, s[10:11], v10, v10, v48
	v_rcp_f32_e32 v12, v11
	s_nop 0
	v_fma_f32 v13, -v11, v12, 1.0
	v_fmac_f32_e32 v12, v13, v12
	v_div_scale_f32 v13, vcc, v48, v10, v48
	v_mul_f32_e32 v14, v13, v12
	v_fma_f32 v15, -v11, v14, v13
	v_fmac_f32_e32 v14, v15, v12
	v_fma_f32 v11, -v11, v14, v13
	v_div_fmas_f32 v11, v11, v12, v14
	v_div_fixup_f32 v48, v11, v10, v48
	ds_write_b32 v3, v48 offset:48
	s_waitcnt vmcnt(6)
	v_mul_f32_e32 v10, 0xbfb8aa3b, v49
	v_exp_f32_e32 v10, v10
	s_nop 0
	v_add_f32_e32 v10, 1.0, v10
	v_div_scale_f32 v11, s[10:11], v10, v10, v49
	v_rcp_f32_e32 v12, v11
	s_nop 0
	v_fma_f32 v13, -v11, v12, 1.0
	v_fmac_f32_e32 v12, v13, v12
	v_div_scale_f32 v13, vcc, v49, v10, v49
	v_mul_f32_e32 v14, v13, v12
	v_fma_f32 v15, -v11, v14, v13
	v_fmac_f32_e32 v14, v15, v12
	v_fma_f32 v11, -v11, v14, v13
	v_div_fmas_f32 v11, v11, v12, v14
	v_div_fixup_f32 v49, v11, v10, v49
	ds_write_b32 v3, v49 offset:32816
	s_waitcnt vmcnt(5)
	v_mul_f32_e32 v10, 0xbfb8aa3b, v50
	v_exp_f32_e32 v10, v10
	s_nop 0
	v_add_f32_e32 v10, 1.0, v10
	v_div_scale_f32 v11, s[10:11], v10, v10, v50
	v_rcp_f32_e32 v12, v11
	s_nop 0
	v_fma_f32 v13, -v11, v12, 1.0
	v_fmac_f32_e32 v12, v13, v12
	v_div_scale_f32 v13, vcc, v50, v10, v50
	v_mul_f32_e32 v14, v13, v12
	v_fma_f32 v15, -v11, v14, v13
	v_fmac_f32_e32 v14, v15, v12
	v_fma_f32 v11, -v11, v14, v13
	v_div_fmas_f32 v11, v11, v12, v14
	v_div_fixup_f32 v50, v11, v10, v50
	ds_write_b32 v3, v50 offset:52
	s_waitcnt vmcnt(4)
	v_mul_f32_e32 v10, 0xbfb8aa3b, v51
	v_exp_f32_e32 v10, v10
	s_nop 0
	v_add_f32_e32 v10, 1.0, v10
	v_div_scale_f32 v11, s[10:11], v10, v10, v51
	v_rcp_f32_e32 v12, v11
	s_nop 0
	v_fma_f32 v13, -v11, v12, 1.0
	v_fmac_f32_e32 v12, v13, v12
	v_div_scale_f32 v13, vcc, v51, v10, v51
	v_mul_f32_e32 v14, v13, v12
	v_fma_f32 v15, -v11, v14, v13
	v_fmac_f32_e32 v14, v15, v12
	v_fma_f32 v11, -v11, v14, v13
	v_div_fmas_f32 v11, v11, v12, v14
	v_div_fixup_f32 v51, v11, v10, v51
	ds_write_b32 v3, v51 offset:32820
	s_waitcnt vmcnt(3)
	v_mul_f32_e32 v10, 0xbfb8aa3b, v52
	v_exp_f32_e32 v10, v10
	s_nop 0
	v_add_f32_e32 v10, 1.0, v10
	v_div_scale_f32 v11, s[10:11], v10, v10, v52
	v_rcp_f32_e32 v12, v11
	s_nop 0
	v_fma_f32 v13, -v11, v12, 1.0
	v_fmac_f32_e32 v12, v13, v12
	v_div_scale_f32 v13, vcc, v52, v10, v52
	v_mul_f32_e32 v14, v13, v12
	v_fma_f32 v15, -v11, v14, v13
	v_fmac_f32_e32 v14, v15, v12
	v_fma_f32 v11, -v11, v14, v13
	v_div_fmas_f32 v11, v11, v12, v14
	v_div_fixup_f32 v52, v11, v10, v52
	ds_write_b32 v3, v52 offset:56
	s_waitcnt vmcnt(2)
	v_mul_f32_e32 v10, 0xbfb8aa3b, v53
	v_exp_f32_e32 v10, v10
	s_nop 0
	v_add_f32_e32 v10, 1.0, v10
	v_div_scale_f32 v11, s[10:11], v10, v10, v53
	v_rcp_f32_e32 v12, v11
	s_nop 0
	v_fma_f32 v13, -v11, v12, 1.0
	v_fmac_f32_e32 v12, v13, v12
	v_div_scale_f32 v13, vcc, v53, v10, v53
	v_mul_f32_e32 v14, v13, v12
	v_fma_f32 v15, -v11, v14, v13
	v_fmac_f32_e32 v14, v15, v12
	v_fma_f32 v11, -v11, v14, v13
	v_div_fmas_f32 v11, v11, v12, v14
	v_div_fixup_f32 v53, v11, v10, v53
	ds_write_b32 v3, v53 offset:32824
	s_waitcnt vmcnt(1)
	v_mul_f32_e32 v10, 0xbfb8aa3b, v54
	v_exp_f32_e32 v10, v10
	s_nop 0
	v_add_f32_e32 v10, 1.0, v10
	v_div_scale_f32 v11, s[10:11], v10, v10, v54
	v_rcp_f32_e32 v12, v11
	s_nop 0
	v_fma_f32 v13, -v11, v12, 1.0
	v_fmac_f32_e32 v12, v13, v12
	v_div_scale_f32 v13, vcc, v54, v10, v54
	v_mul_f32_e32 v14, v13, v12
	v_fma_f32 v15, -v11, v14, v13
	v_fmac_f32_e32 v14, v15, v12
	v_fma_f32 v11, -v11, v14, v13
	v_div_fmas_f32 v11, v11, v12, v14
	v_div_fixup_f32 v54, v11, v10, v54
	ds_write_b32 v3, v54 offset:60
	s_waitcnt vmcnt(0)
	v_mul_f32_e32 v10, 0xbfb8aa3b, v55
	v_exp_f32_e32 v10, v10
	s_nop 0
	v_add_f32_e32 v10, 1.0, v10
	v_div_scale_f32 v11, s[10:11], v10, v10, v55
	v_rcp_f32_e32 v12, v11
	s_nop 0
	v_fma_f32 v13, -v11, v12, 1.0
	v_fmac_f32_e32 v12, v13, v12
	v_div_scale_f32 v13, vcc, v55, v10, v55
	v_mul_f32_e32 v14, v13, v12
	v_fma_f32 v15, -v11, v14, v13
	v_fmac_f32_e32 v14, v15, v12
	v_fma_f32 v11, -v11, v14, v13
	v_div_fmas_f32 v11, v11, v12, v14
	v_div_fixup_f32 v55, v11, v10, v55
	ds_write_b32 v3, v55 offset:32828
